# v5 with the in-projection Z stores using the default cache policy instead of nt
# speedup vs baseline: 1.0087x; 1.0081x over previous
.LBB0_293:
	s_lshl_b32 s18, s54, 8
	s_add_i32 s19, s18, 0x800
	s_cmp_lt_i32 s54, 24
	s_cselect_b32 s18, s18, s19
	v_or_b32_e32 v4, s18, v200
	v_ashrrev_i32_e32 v5, 31, v4
	v_mov_b64_e32 v[2:3], s[0:1]
	v_mad_i64_i32 v[8:9], s[58:59], v6, s35, v[2:3]
	v_lshlrev_b64 v[4:5], 1, v[4:5]
	v_lshl_add_u64 v[12:13], v[8:9], 0, v[4:5]
	v_pk_mul_f32 v[8:9], v[158:159], s[38:39] op_sel_hi:[1,0]
	v_pk_mul_f32 v[10:11], v[160:161], s[38:39] op_sel_hi:[1,0]
	v_cvt_pk_bf16_f32 v8, v8, v9
	v_pk_mul_f32 v[14:15], v[156:157], s[38:39] op_sel_hi:[1,0]
	v_cvt_pk_bf16_f32 v9, v10, v11
	v_pk_mul_f32 v[16:17], v[154:155], s[38:39] op_sel_hi:[1,0]
	v_or_b32_e32 v7, 16, v6
	v_cvt_pk_bf16_f32 v10, v16, v17
	v_cvt_pk_bf16_f32 v11, v14, v15
	global_store_dwordx4 v[12:13], v[8:11], off
	v_pk_mul_f32 v[14:15], v[140:141], s[38:39] op_sel_hi:[1,0]
	v_pk_mul_f32 v[16:17], v[138:139], s[38:39] op_sel_hi:[1,0]
	v_pk_mul_f32 v[8:9], v[142:143], s[38:39] op_sel_hi:[1,0]
	v_pk_mul_f32 v[10:11], v[144:145], s[38:39] op_sel_hi:[1,0]
	v_cvt_pk_bf16_f32 v8, v8, v9
	s_nop 0
	v_cvt_pk_bf16_f32 v9, v10, v11
	v_cvt_pk_bf16_f32 v10, v16, v17
	v_cvt_pk_bf16_f32 v11, v14, v15
	global_store_dwordx4 v[12:13], v[8:11], off offset:256
	v_pk_mul_f32 v[14:15], v[148:149], s[38:39] op_sel_hi:[1,0]
	v_pk_mul_f32 v[16:17], v[146:147], s[38:39] op_sel_hi:[1,0]
	v_mad_i64_i32 v[8:9], s[58:59], v7, s35, v[2:3]
	v_lshl_add_u64 v[12:13], v[8:9], 0, v[4:5]
	v_pk_mul_f32 v[8:9], v[150:151], s[38:39] op_sel_hi:[1,0]
	v_pk_mul_f32 v[10:11], v[152:153], s[38:39] op_sel_hi:[1,0]
	v_cvt_pk_bf16_f32 v8, v8, v9
	v_or_b32_e32 v7, 32, v6
	v_cvt_pk_bf16_f32 v9, v10, v11
	v_cvt_pk_bf16_f32 v10, v16, v17
	v_cvt_pk_bf16_f32 v11, v14, v15
	global_store_dwordx4 v[12:13], v[8:11], off
	v_pk_mul_f32 v[14:15], v[128:129], s[38:39] op_sel_hi:[1,0]
	v_pk_mul_f32 v[16:17], v[126:127], s[38:39] op_sel_hi:[1,0]
	v_pk_mul_f32 v[8:9], v[134:135], s[38:39] op_sel_hi:[1,0]
	v_pk_mul_f32 v[10:11], v[136:137], s[38:39] op_sel_hi:[1,0]
	v_cvt_pk_bf16_f32 v8, v8, v9
	s_nop 0
	v_cvt_pk_bf16_f32 v9, v10, v11
	v_cvt_pk_bf16_f32 v10, v16, v17
	v_cvt_pk_bf16_f32 v11, v14, v15
	global_store_dwordx4 v[12:13], v[8:11], off offset:256
	v_pk_mul_f32 v[14:15], v[124:125], s[38:39] op_sel_hi:[1,0]
	v_pk_mul_f32 v[16:17], v[122:123], s[38:39] op_sel_hi:[1,0]
	v_mad_i64_i32 v[8:9], s[58:59], v7, s35, v[2:3]
	v_lshl_add_u64 v[12:13], v[8:9], 0, v[4:5]
	v_pk_mul_f32 v[8:9], v[130:131], s[38:39] op_sel_hi:[1,0]
	v_pk_mul_f32 v[10:11], v[132:133], s[38:39] op_sel_hi:[1,0]
	v_cvt_pk_bf16_f32 v8, v8, v9
	v_or_b32_e32 v7, 48, v6
	v_cvt_pk_bf16_f32 v9, v10, v11
	v_cvt_pk_bf16_f32 v10, v16, v17
	v_cvt_pk_bf16_f32 v11, v14, v15
	global_store_dwordx4 v[12:13], v[8:11], off
	v_pk_mul_f32 v[14:15], v[108:109], s[38:39] op_sel_hi:[1,0]
	v_pk_mul_f32 v[16:17], v[106:107], s[38:39] op_sel_hi:[1,0]
	v_pk_mul_f32 v[8:9], v[110:111], s[38:39] op_sel_hi:[1,0]
	v_pk_mul_f32 v[10:11], v[112:113], s[38:39] op_sel_hi:[1,0]
	v_cvt_pk_bf16_f32 v8, v8, v9
	s_nop 0
	v_cvt_pk_bf16_f32 v9, v10, v11
	v_cvt_pk_bf16_f32 v10, v16, v17
	v_cvt_pk_bf16_f32 v11, v14, v15
	global_store_dwordx4 v[12:13], v[8:11], off offset:256
	v_pk_mul_f32 v[14:15], v[116:117], s[38:39] op_sel_hi:[1,0]
	v_pk_mul_f32 v[16:17], v[114:115], s[38:39] op_sel_hi:[1,0]
	v_mad_i64_i32 v[8:9], s[58:59], v7, s35, v[2:3]
	v_lshl_add_u64 v[12:13], v[8:9], 0, v[4:5]
	v_pk_mul_f32 v[8:9], v[118:119], s[38:39] op_sel_hi:[1,0]
	v_pk_mul_f32 v[10:11], v[120:121], s[38:39] op_sel_hi:[1,0]
	v_cvt_pk_bf16_f32 v8, v8, v9
	v_add_u32_e32 v7, 0x80, v6
	v_cvt_pk_bf16_f32 v9, v10, v11
	v_cvt_pk_bf16_f32 v10, v16, v17
	v_cvt_pk_bf16_f32 v11, v14, v15
	global_store_dwordx4 v[12:13], v[8:11], off
	v_pk_mul_f32 v[14:15], v[100:101], s[38:39] op_sel_hi:[1,0]
	v_pk_mul_f32 v[16:17], v[98:99], s[38:39] op_sel_hi:[1,0]
	v_pk_mul_f32 v[8:9], v[102:103], s[38:39] op_sel_hi:[1,0]
	v_pk_mul_f32 v[10:11], v[104:105], s[38:39] op_sel_hi:[1,0]
	v_cvt_pk_bf16_f32 v8, v8, v9
	s_nop 0
	v_cvt_pk_bf16_f32 v9, v10, v11
	v_cvt_pk_bf16_f32 v10, v16, v17
	v_cvt_pk_bf16_f32 v11, v14, v15
	global_store_dwordx4 v[12:13], v[8:11], off offset:256
	v_pk_mul_f32 v[14:15], v[92:93], s[38:39] op_sel_hi:[1,0]
	v_pk_mul_f32 v[16:17], v[90:91], s[38:39] op_sel_hi:[1,0]
	v_mad_i64_i32 v[8:9], s[58:59], v7, s35, v[2:3]
	v_lshl_add_u64 v[12:13], v[8:9], 0, v[4:5]
	v_pk_mul_f32 v[8:9], v[94:95], s[38:39] op_sel_hi:[1,0]
	v_pk_mul_f32 v[10:11], v[96:97], s[38:39] op_sel_hi:[1,0]
	v_cvt_pk_bf16_f32 v8, v8, v9
	v_add_u32_e32 v7, 0x90, v6
	v_cvt_pk_bf16_f32 v9, v10, v11
	v_cvt_pk_bf16_f32 v10, v16, v17
	v_cvt_pk_bf16_f32 v11, v14, v15
	global_store_dwordx4 v[12:13], v[8:11], off
	v_pk_mul_f32 v[14:15], v[76:77], s[38:39] op_sel_hi:[1,0]
	v_pk_mul_f32 v[16:17], v[74:75], s[38:39] op_sel_hi:[1,0]
	v_pk_mul_f32 v[8:9], v[78:79], s[38:39] op_sel_hi:[1,0]
	v_pk_mul_f32 v[10:11], v[80:81], s[38:39] op_sel_hi:[1,0]
	v_cvt_pk_bf16_f32 v8, v8, v9
	s_nop 0
	v_cvt_pk_bf16_f32 v9, v10, v11
	v_cvt_pk_bf16_f32 v10, v16, v17
	v_cvt_pk_bf16_f32 v11, v14, v15
	global_store_dwordx4 v[12:13], v[8:11], off offset:256
	v_pk_mul_f32 v[14:15], v[84:85], s[38:39] op_sel_hi:[1,0]
	v_pk_mul_f32 v[16:17], v[82:83], s[38:39] op_sel_hi:[1,0]
	v_mad_i64_i32 v[8:9], s[58:59], v7, s35, v[2:3]
	v_lshl_add_u64 v[12:13], v[8:9], 0, v[4:5]
	v_pk_mul_f32 v[8:9], v[86:87], s[38:39] op_sel_hi:[1,0]
	v_pk_mul_f32 v[10:11], v[88:89], s[38:39] op_sel_hi:[1,0]
	v_cvt_pk_bf16_f32 v8, v8, v9
	v_add_u32_e32 v7, 0xa0, v6
	v_cvt_pk_bf16_f32 v9, v10, v11
	v_cvt_pk_bf16_f32 v10, v16, v17
	v_cvt_pk_bf16_f32 v11, v14, v15
	global_store_dwordx4 v[12:13], v[8:11], off
	v_pk_mul_f32 v[14:15], v[64:65], s[38:39] op_sel_hi:[1,0]
	v_pk_mul_f32 v[16:17], v[62:63], s[38:39] op_sel_hi:[1,0]
	v_pk_mul_f32 v[8:9], v[70:71], s[38:39] op_sel_hi:[1,0]
	v_pk_mul_f32 v[10:11], v[72:73], s[38:39] op_sel_hi:[1,0]
	v_cvt_pk_bf16_f32 v8, v8, v9
	s_nop 0
	v_cvt_pk_bf16_f32 v9, v10, v11
	v_cvt_pk_bf16_f32 v10, v16, v17
	v_cvt_pk_bf16_f32 v11, v14, v15
	global_store_dwordx4 v[12:13], v[8:11], off offset:256
	v_pk_mul_f32 v[14:15], v[60:61], s[38:39] op_sel_hi:[1,0]
	v_pk_mul_f32 v[16:17], v[58:59], s[38:39] op_sel_hi:[1,0]
	v_mad_i64_i32 v[8:9], s[58:59], v7, s35, v[2:3]
	v_lshl_add_u64 v[12:13], v[8:9], 0, v[4:5]
	v_pk_mul_f32 v[8:9], v[66:67], s[38:39] op_sel_hi:[1,0]
	v_pk_mul_f32 v[10:11], v[68:69], s[38:39] op_sel_hi:[1,0]
	v_cvt_pk_bf16_f32 v8, v8, v9
	v_add_u32_e32 v7, 0xb0, v6
	v_cvt_pk_bf16_f32 v9, v10, v11
	v_cvt_pk_bf16_f32 v10, v16, v17
	v_cvt_pk_bf16_f32 v11, v14, v15
	global_store_dwordx4 v[12:13], v[8:11], off
	v_mad_i64_i32 v[2:3], s[58:59], v7, s35, v[2:3]
	s_nop 0
	v_pk_mul_f32 v[8:9], v[46:47], s[38:39] op_sel_hi:[1,0]
	v_pk_mul_f32 v[10:11], v[48:49], s[38:39] op_sel_hi:[1,0]
	v_cvt_pk_bf16_f32 v8, v8, v9
	v_pk_mul_f32 v[14:15], v[44:45], s[38:39] op_sel_hi:[1,0]
	v_cvt_pk_bf16_f32 v9, v10, v11
	v_pk_mul_f32 v[16:17], v[42:43], s[38:39] op_sel_hi:[1,0]
	s_nop 0
	v_cvt_pk_bf16_f32 v10, v16, v17
	v_cvt_pk_bf16_f32 v11, v14, v15
	global_store_dwordx4 v[12:13], v[8:11], off offset:256
	v_pk_mul_f32 v[12:13], v[50:51], s[38:39] op_sel_hi:[1,0]
	s_nop 0
	v_lshl_add_u64 v[8:9], v[2:3], 0, v[4:5]
	v_pk_mul_f32 v[4:5], v[56:57], s[38:39] op_sel_hi:[1,0]
	v_pk_mul_f32 v[2:3], v[54:55], s[38:39] op_sel_hi:[1,0]
	v_pk_mul_f32 v[10:11], v[52:53], s[38:39] op_sel_hi:[1,0]
	v_cvt_pk_bf16_f32 v2, v2, v3
	v_cvt_pk_bf16_f32 v3, v4, v5
	v_cvt_pk_bf16_f32 v4, v12, v13
	v_pk_mul_f32 v[12:13], v[34:35], s[38:39] op_sel_hi:[1,0]
	v_cvt_pk_bf16_f32 v5, v10, v11
	global_store_dwordx4 v[8:9], v[2:5], off
	v_pk_mul_f32 v[10:11], v[36:37], s[38:39] op_sel_hi:[1,0]
	s_nop 0
	v_pk_mul_f32 v[4:5], v[40:41], s[38:39] op_sel_hi:[1,0]
	v_pk_mul_f32 v[2:3], v[38:39], s[38:39] op_sel_hi:[1,0]
	s_nop 0
	v_cvt_pk_bf16_f32 v2, v2, v3
	v_cvt_pk_bf16_f32 v3, v4, v5
	v_cvt_pk_bf16_f32 v4, v12, v13
	v_cvt_pk_bf16_f32 v5, v10, v11
	global_store_dwordx4 v[8:9], v[2:5], off offset:256
	s_cbranch_execnz .LBB0_290

.LBB0_339:
	s_mul_hi_i32 s17, s86, 0x92492493
	s_add_i32 s17, s17, s86
	s_lshr_b32 s18, s17, 31
	s_lshr_b32 s17, s17, 5
	s_add_i32 s17, s17, s18
	s_mul_i32 s17, s17, 56
	s_sub_i32 s17, s86, s17
	v_lshl_or_b32 v144, s17, 8, v148
	v_lshl_add_u32 v151, s46, 8, v146
	v_ashrrev_i32_e32 v145, 31, v144
	v_mov_b64_e32 v[142:143], s[0:1]
	v_mad_i64_i32 v[152:153], s[48:49], v151, s85, v[142:143]
	v_lshlrev_b64 v[144:145], 1, v[144:145]
	v_lshl_add_u64 v[152:153], v[152:153], 0, v[144:145]
	v_pk_add_f32 v[128:129], v[128:129], 0 op_sel_hi:[1,0]
	v_pk_add_f32 v[126:127], v[126:127], 0 op_sel_hi:[1,0]
	v_pk_add_f32 v[154:155], v[124:125], 0 op_sel_hi:[1,0]
	v_pk_add_f32 v[124:125], v[122:123], 0 op_sel_hi:[1,0]
	v_cvt_pk_bf16_f32 v122, v126, v127
	v_cvt_pk_bf16_f32 v123, v128, v129
	v_pk_add_f32 v[118:119], v[118:119], 0 op_sel_hi:[1,0]
	v_cvt_pk_bf16_f32 v124, v124, v125
	v_cvt_pk_bf16_f32 v125, v154, v155
	global_store_dwordx4 v[152:153], v[122:125], off
	v_pk_add_f32 v[120:121], v[120:121], 0 op_sel_hi:[1,0]
	v_pk_add_f32 v[114:115], v[114:115], 0 op_sel_hi:[1,0]
	v_pk_add_f32 v[122:123], v[112:113], 0 op_sel_hi:[1,0]
	v_pk_add_f32 v[112:113], v[110:111], 0 op_sel_hi:[1,0]
	v_cvt_pk_bf16_f32 v110, v118, v119
	v_cvt_pk_bf16_f32 v111, v120, v121
	v_pk_add_f32 v[102:103], v[102:103], 0 op_sel_hi:[1,0]
	v_cvt_pk_bf16_f32 v112, v112, v113
	v_cvt_pk_bf16_f32 v113, v122, v123
	global_store_dwordx4 v[152:153], v[110:113], off offset:256
	v_pk_add_f32 v[104:105], v[104:105], 0 op_sel_hi:[1,0]
	v_pk_add_f32 v[98:99], v[98:99], 0 op_sel_hi:[1,0]
	v_or_b32_e32 v110, 16, v151
	v_mad_i64_i32 v[110:111], s[48:49], v110, s85, v[142:143]
	v_lshl_add_u64 v[110:111], v[110:111], 0, v[144:145]
	v_pk_add_f32 v[112:113], v[116:117], 0 op_sel_hi:[1,0]
	v_pk_add_f32 v[116:117], v[108:109], 0 op_sel_hi:[1,0]
	v_pk_add_f32 v[108:109], v[106:107], 0 op_sel_hi:[1,0]
	v_cvt_pk_bf16_f32 v106, v114, v115
	v_cvt_pk_bf16_f32 v107, v112, v113
	v_pk_add_f32 v[86:87], v[86:87], 0 op_sel_hi:[1,0]
	v_cvt_pk_bf16_f32 v108, v108, v109
	v_cvt_pk_bf16_f32 v109, v116, v117
	global_store_dwordx4 v[110:111], v[106:109], off
	v_pk_add_f32 v[88:89], v[88:89], 0 op_sel_hi:[1,0]
	v_pk_add_f32 v[82:83], v[82:83], 0 op_sel_hi:[1,0]
	v_pk_add_f32 v[106:107], v[96:97], 0 op_sel_hi:[1,0]
	v_pk_add_f32 v[96:97], v[94:95], 0 op_sel_hi:[1,0]
	v_cvt_pk_bf16_f32 v94, v102, v103
	v_cvt_pk_bf16_f32 v95, v104, v105
	v_pk_add_f32 v[70:71], v[70:71], 0 op_sel_hi:[1,0]
	v_cvt_pk_bf16_f32 v96, v96, v97
	v_cvt_pk_bf16_f32 v97, v106, v107
	global_store_dwordx4 v[110:111], v[94:97], off offset:256
	v_pk_add_f32 v[72:73], v[72:73], 0 op_sel_hi:[1,0]
	v_pk_add_f32 v[64:65], v[64:65], 0 op_sel_hi:[1,0]
	v_or_b32_e32 v94, 32, v151
	v_mad_i64_i32 v[94:95], s[48:49], v94, s85, v[142:143]
	v_lshl_add_u64 v[94:95], v[94:95], 0, v[144:145]
	v_pk_add_f32 v[96:97], v[100:101], 0 op_sel_hi:[1,0]
	v_pk_add_f32 v[100:101], v[92:93], 0 op_sel_hi:[1,0]
	v_pk_add_f32 v[92:93], v[90:91], 0 op_sel_hi:[1,0]
	v_cvt_pk_bf16_f32 v90, v98, v99
	v_cvt_pk_bf16_f32 v91, v96, v97
	v_pk_add_f32 v[62:63], v[62:63], 0 op_sel_hi:[1,0]
	v_cvt_pk_bf16_f32 v92, v92, v93
	v_cvt_pk_bf16_f32 v93, v100, v101
	global_store_dwordx4 v[94:95], v[90:93], off
	v_pk_add_f32 v[54:55], v[54:55], 0 op_sel_hi:[1,0]
	v_pk_add_f32 v[56:57], v[56:57], 0 op_sel_hi:[1,0]
	v_pk_add_f32 v[90:91], v[80:81], 0 op_sel_hi:[1,0]
	v_pk_add_f32 v[80:81], v[78:79], 0 op_sel_hi:[1,0]
	v_cvt_pk_bf16_f32 v78, v86, v87
	v_cvt_pk_bf16_f32 v79, v88, v89
	v_pk_add_f32 v[50:51], v[50:51], 0 op_sel_hi:[1,0]
	v_cvt_pk_bf16_f32 v80, v80, v81
	v_cvt_pk_bf16_f32 v81, v90, v91
	global_store_dwordx4 v[94:95], v[78:81], off offset:256
	v_pk_add_f32 v[38:39], v[38:39], 0 op_sel_hi:[1,0]
	v_pk_add_f32 v[40:41], v[40:41], 0 op_sel_hi:[1,0]
	v_or_b32_e32 v78, 48, v151
	v_mad_i64_i32 v[78:79], s[48:49], v78, s85, v[142:143]
	v_lshl_add_u64 v[78:79], v[78:79], 0, v[144:145]
	v_pk_add_f32 v[80:81], v[84:85], 0 op_sel_hi:[1,0]
	v_pk_add_f32 v[84:85], v[76:77], 0 op_sel_hi:[1,0]
	v_pk_add_f32 v[76:77], v[74:75], 0 op_sel_hi:[1,0]
	v_cvt_pk_bf16_f32 v74, v82, v83
	v_cvt_pk_bf16_f32 v75, v80, v81
	v_pk_add_f32 v[34:35], v[34:35], 0 op_sel_hi:[1,0]
	v_cvt_pk_bf16_f32 v76, v76, v77
	v_cvt_pk_bf16_f32 v77, v84, v85
	global_store_dwordx4 v[78:79], v[74:77], off
	v_pk_add_f32 v[22:23], v[22:23], 0 op_sel_hi:[1,0]
	v_pk_add_f32 v[24:25], v[24:25], 0 op_sel_hi:[1,0]
	v_pk_add_f32 v[74:75], v[68:69], 0 op_sel_hi:[1,0]
	v_pk_add_f32 v[68:69], v[66:67], 0 op_sel_hi:[1,0]
	v_cvt_pk_bf16_f32 v66, v70, v71
	v_cvt_pk_bf16_f32 v67, v72, v73
	v_pk_add_f32 v[18:19], v[18:19], 0 op_sel_hi:[1,0]
	v_cvt_pk_bf16_f32 v68, v68, v69
	v_cvt_pk_bf16_f32 v69, v74, v75
	global_store_dwordx4 v[78:79], v[66:69], off offset:256
	s_andn2_b64 vcc, exec, s[42:43]
	v_pk_add_f32 v[8:9], v[8:9], 0 op_sel_hi:[1,0]
	v_add_u32_e32 v66, 0x80, v151
	v_mad_i64_i32 v[66:67], s[48:49], v66, s85, v[142:143]
	v_lshl_add_u64 v[66:67], v[66:67], 0, v[144:145]
	v_pk_add_f32 v[68:69], v[60:61], 0 op_sel_hi:[1,0]
	v_pk_add_f32 v[60:61], v[58:59], 0 op_sel_hi:[1,0]
	v_cvt_pk_bf16_f32 v58, v62, v63
	v_cvt_pk_bf16_f32 v59, v64, v65
	v_pk_add_f32 v[6:7], v[6:7], 0 op_sel_hi:[1,0]
	v_cvt_pk_bf16_f32 v60, v60, v61
	v_cvt_pk_bf16_f32 v61, v68, v69
	global_store_dwordx4 v[66:67], v[58:61], off
	s_nop 1
	v_pk_add_f32 v[58:59], v[48:49], 0 op_sel_hi:[1,0]
	v_pk_add_f32 v[48:49], v[46:47], 0 op_sel_hi:[1,0]
	v_cvt_pk_bf16_f32 v46, v54, v55
	v_cvt_pk_bf16_f32 v47, v56, v57
	s_nop 0
	v_cvt_pk_bf16_f32 v48, v48, v49
	v_cvt_pk_bf16_f32 v49, v58, v59
	global_store_dwordx4 v[66:67], v[46:49], off offset:256
	s_nop 1
	v_add_u32_e32 v46, 0x90, v151
	v_mad_i64_i32 v[46:47], s[48:49], v46, s85, v[142:143]
	v_lshl_add_u64 v[46:47], v[46:47], 0, v[144:145]
	v_pk_add_f32 v[48:49], v[52:53], 0 op_sel_hi:[1,0]
	v_pk_add_f32 v[52:53], v[44:45], 0 op_sel_hi:[1,0]
	v_pk_add_f32 v[44:45], v[42:43], 0 op_sel_hi:[1,0]
	v_cvt_pk_bf16_f32 v42, v50, v51
	v_cvt_pk_bf16_f32 v43, v48, v49
	s_nop 0
	v_cvt_pk_bf16_f32 v44, v44, v45
	v_cvt_pk_bf16_f32 v45, v52, v53
	global_store_dwordx4 v[46:47], v[42:45], off
	s_nop 1
	v_pk_add_f32 v[42:43], v[32:33], 0 op_sel_hi:[1,0]
	v_pk_add_f32 v[32:33], v[30:31], 0 op_sel_hi:[1,0]
	v_cvt_pk_bf16_f32 v30, v38, v39
	v_cvt_pk_bf16_f32 v31, v40, v41
	s_nop 0
	v_cvt_pk_bf16_f32 v32, v32, v33
	v_cvt_pk_bf16_f32 v33, v42, v43
	global_store_dwordx4 v[46:47], v[30:33], off offset:256
	s_nop 1
	v_add_u32_e32 v30, 0xa0, v151
	v_mad_i64_i32 v[30:31], s[48:49], v30, s85, v[142:143]
	v_lshl_add_u64 v[30:31], v[30:31], 0, v[144:145]
	v_pk_add_f32 v[32:33], v[36:37], 0 op_sel_hi:[1,0]
	v_pk_add_f32 v[36:37], v[28:29], 0 op_sel_hi:[1,0]
	v_pk_add_f32 v[28:29], v[26:27], 0 op_sel_hi:[1,0]
	v_cvt_pk_bf16_f32 v26, v34, v35
	v_cvt_pk_bf16_f32 v27, v32, v33
	s_nop 0
	v_cvt_pk_bf16_f32 v28, v28, v29
	v_cvt_pk_bf16_f32 v29, v36, v37
	global_store_dwordx4 v[30:31], v[26:29], off
	s_nop 1
	v_pk_add_f32 v[26:27], v[16:17], 0 op_sel_hi:[1,0]
	v_pk_add_f32 v[16:17], v[14:15], 0 op_sel_hi:[1,0]
	v_cvt_pk_bf16_f32 v14, v22, v23
	v_cvt_pk_bf16_f32 v15, v24, v25
	s_nop 0
	v_cvt_pk_bf16_f32 v16, v16, v17
	v_cvt_pk_bf16_f32 v17, v26, v27
	global_store_dwordx4 v[30:31], v[14:17], off offset:256
	s_nop 1
	v_add_u32_e32 v14, 0xb0, v151
	v_mad_i64_i32 v[14:15], s[48:49], v14, s85, v[142:143]
	v_lshl_add_u64 v[14:15], v[14:15], 0, v[144:145]
	v_pk_add_f32 v[16:17], v[20:21], 0 op_sel_hi:[1,0]
	v_pk_add_f32 v[20:21], v[12:13], 0 op_sel_hi:[1,0]
	v_pk_add_f32 v[12:13], v[10:11], 0 op_sel_hi:[1,0]
	v_cvt_pk_bf16_f32 v10, v18, v19
	v_cvt_pk_bf16_f32 v11, v16, v17
	s_nop 0
	v_cvt_pk_bf16_f32 v12, v12, v13
	v_cvt_pk_bf16_f32 v13, v20, v21
	global_store_dwordx4 v[14:15], v[10:13], off
	s_nop 1
	v_pk_add_f32 v[10:11], v[4:5], 0 op_sel_hi:[1,0]
	v_pk_add_f32 v[4:5], v[2:3], 0 op_sel_hi:[1,0]
	v_cvt_pk_bf16_f32 v2, v6, v7
	v_cvt_pk_bf16_f32 v3, v8, v9
	s_nop 0
	v_cvt_pk_bf16_f32 v4, v4, v5
	v_cvt_pk_bf16_f32 v5, v10, v11
	global_store_dwordx4 v[14:15], v[2:5], off offset:256
	s_cbranch_vccnz .LBB0_342
	s_andn2_b64 vcc, exec, s[10:11]
	s_cbranch_vccnz .LBB0_315
	s_barrier
	s_branch .LBB0_315
